# P4a: second weight tile (waves 0-3) also fetched one load at a time across the later doubling levels (exec-masked)
# baseline (speedup 1.0000x reference)
; __device__ __forceinline__ void tr8_load(const MoeItem& m, f32x4 (&v)[16], int lane) {
;     const int kr = lane >> 4, cq = lane & 15;
;     const int voff = (kr * m.ldw + 4 * cq) * 4;
; #pragma unroll
;     for (int i = 0; i < 16; ++i) v[i] = __builtin_bit_cast(f32x4, __builtin_amdgcn_raw_buffer_load_b128(m.rs, voff, (int)(m.soff + (unsigned)i * m.rstep), 0));
; }
; __device__ __forceinline__ MoeItem moe_item(int r, const float* w_gu, const float* w_down, unsigned char* ws) {
;     MoeItem m;
;     if (r < MOE_J4) { const int e = r / 2048, q = r % 2048, kb = q / 64, cb = q % 64, c0 = cb * 64; const int cc = c0 & 2047;
;         m.rs = __builtin_amdgcn_make_buffer_rsrc((void*)w_gu, 0, 0xffffffff, 0x00020000); m.ldw = 2 * FF; m.k0 = kb * 64;
;         m.soff = (unsigned)(((size_t)e * D * 2 * FF + (size_t)kb * 64 * (2 * FF) + c0) * 4); m.rstep = 4u * (2 * FF) * 4u;
;         m.WT = ws + WS_WGUT + (size_t)e * 2 * FF * D; m.ldt = D; m.drow = (cc >> 7) * 256 + (c0 >= 2048 ? 128 : 0) + (cc & 127); }
;     else { r -= MOE_J4; const int e = r / 1024, q = r % 1024, kb = q / 32, cb = q % 32;
;         m.rs = __builtin_amdgcn_make_buffer_rsrc((void*)w_down, 0, 0xffffffff, 0x00020000); m.ldw = D; m.k0 = kb * 64;
;         m.soff = (unsigned)(((size_t)e * FF * D + (size_t)kb * 64 * D + cb * 64) * 4); m.rstep = 4u * D * 4u;
;         m.WT = ws + WS_WDNT + (size_t)e * D * FF; m.ldt = FF; m.drow = cb * 64; }
;     return m;
; __device__ __forceinline__ void p4a_chunk(Frame& F0, const In& I) {
;     ...
;             if (lvl == 2) { if (hx) tr8_finish(tX, mX, tscr, lane);
;                             if (hy) { mX = moe_item(cit + 8, I.w_gu, I.w_down, F.ws); tr8_load(mX, tX, lane); } }
.LBB0_1094:
	v_cndmask_b32_e64 v68, 0, 1, s[70:71]
	v_cmp_ne_u32_e64 s[64:65], 1, v68
	s_andn2_b64 vcc, exec, s[70:71]
	s_cbranch_vccnz .LBB0_1096
	s_add_i32 s16, s85, 8
	s_add_i32 s14, s85, 0xffff0008
	s_lshr_b32 s86, s14, 10
	s_bfe_u32 s17, s16, 0x50005
	s_lshl_b64 s[14:15], s[86:87], 22
	s_lshl_b32 s72, s17, 17
	s_and_b32 s74, s91, 0x7c0
	s_or_b32 s72, s72, s14
	s_or_b32 s72, s72, s74
	s_add_u32 s75, s68, s14
	s_addc_u32 s73, s69, s15
	s_ashr_i32 s14, s16, 31
	s_lshr_b32 s14, s14, 21
	s_add_i32 s15, s16, s14
	s_ashr_i32 s14, s15, 11
	s_and_b32 s15, s15, 0xf800
	s_sub_i32 s15, s16, s15
	s_sext_i32_i16 s16, s15
	s_bfe_u32 s16, s16, 0x60019
	s_add_i32 s16, s15, s16
	s_sext_i32_i16 s86, s16
	s_and_b32 s16, s16, 0xffc0
	s_ashr_i32 s86, s86, 6
	s_sub_i32 s15, s15, s16
	s_sext_i32_i16 s16, s15
	s_lshl_b32 s93, s14, 23
	s_lshl_b32 vcc_lo, s86, 18
	s_lshl_b32 s92, s16, 6
	s_ashr_i32 s15, s14, 31
	s_add_i32 s93, vcc_lo, s93
	s_add_i32 s93, s93, s92
	s_lshl_b64 s[14:15], s[14:15], 23
	s_add_u32 s14, s80, s14
	v_readlane_b32 s20, v255, 13
	s_addc_u32 s15, s20, s15
	s_lshl_b32 vcc_lo, s16, 7
	s_and_b32 vcc_lo, vcc_lo, 0xf00
	s_cmp_gt_i32 s16, 31
	s_cselect_b32 s16, 0x80, 0
	s_or_b32 s16, vcc_lo, s16
	s_and_b32 s92, s92, 64
	s_or_b32 s16, s16, s92
	s_cmp_lt_i32 s85, 0xfff8
	s_cselect_b32 vcc_hi, s93, s72
	s_mov_b32 s93, 0xa0000
	v_readlane_b32 s48, v254, 37
	s_cselect_b32 s20, s93, 0x50000
	s_mov_b32 s93, 0xc0000
	v_readlane_b32 s49, v254, 38
	v_readlane_b32 s52, v254, 41
	v_readlane_b32 s53, v254, 42
	v_readlane_b32 s54, v254, 43
	s_mov_b32 s72, 0x10000
	s_mov_b32 s48, s22
	s_cselect_b32 s22, s93, 0x60000
	s_mov_b32 s93, 0xe0000
	v_readlane_b32 s50, v254, 39
	v_readlane_b32 s51, v254, 40
	v_readlane_b32 s58, v254, 47
	v_readlane_b32 s59, v254, 48
	v_readlane_b32 s62, v254, 51
	v_readlane_b32 s63, v254, 52
	s_mov_b32 s52, s68
	s_cselect_b32 s68, s72, 0x8000
	s_cselect_b32 s17, s86, s17
	s_cselect_b32 s73, s15, s73
	s_cselect_b32 s72, s14, s75
	s_cselect_b32 s86, s16, s74
	s_cselect_b32 s14, 12, 11
	s_mov_b32 s15, 0x30000
	s_mov_b32 s16, 0x50000
	s_mov_b32 s53, s69
	s_mov_b32 s69, 0x60000
	s_mov_b32 s74, 0x70000
	s_mov_b32 s75, 0x90000
	s_mov_b32 s21, 0xb0000
	s_mov_b32 s49, s23
	s_mov_b32 s23, 0xd0000
	s_mov_b32 s54, s80
	s_cselect_b32 s80, s93, 0x70000
	s_mov_b32 s93, 0xf0000
	s_cselect_b32 s92, s58, s62
	s_cselect_b32 vcc_lo, s59, s63
	s_cselect_b32 s15, s15, 0x18000
	s_cselect_b32 s16, s16, 0x28000
	s_cselect_b32 s69, s69, 0x30000
	s_cselect_b32 s74, s74, 0x38000
	s_cselect_b32 s75, s75, 0x48000
	s_cselect_b32 s21, s21, 0x58000
	s_cselect_b32 s23, s23, 0x68000
	s_mov_b64 s[50:51], s[24:25]
	s_cselect_b32 s24, s93, 0x78000
	s_lshl_b32 s25, vcc_hi, 2
	s_nop 0
	v_lshl_or_b32 v2, v116, s14, v128
	s_and_b32 s93, vcc_lo, 0xffff
	s_nop 0
	v_lshlrev_b32_e32 v62, 2, v2
	s_add_i32 s14, s25, s68
	v_mov_b32_e32 v248, v62
	v_mov_b32_e32 v249, 0
	v_mov_b32_e32 v250, s68
	v_mov_b32_e32 v251, 0
	v_lshl_add_u64 v[248:249], v[248:249], 0, s[92:93]
	v_add_co_u32_e32 v248, vcc, s25, v248
	v_addc_co_u32_e32 v249, vcc, 0, v249, vcc
	global_load_dwordx4 v[2:5], v[248:249], off
	s_add_i32 s14, s14, s68
	s_add_i32 s15, s25, s15
	s_add_i32 vcc_hi, vcc_hi, s68
	s_lshl_b32 s15, vcc_hi, 2
	s_mul_i32 s68, s68, 6
	s_add_i32 s16, s25, s16
	s_add_i32 s15, s25, s69
	s_add_i32 s14, s14, s68
	s_add_i32 s16, s25, s74
	s_add_i32 s15, s25, s75
	s_add_i32 s14, s25, s20
	s_add_i32 s15, s25, s21
	s_add_i32 s14, s25, s22
	s_add_i32 s15, s25, s23
	s_add_i32 s14, s25, s80
	s_add_i32 s25, s25, s24
	s_nop 0
	s_mov_b32 s69, s53
	s_mov_b32 s68, s52
	s_mov_b32 s22, s48
	s_mov_b32 s23, s49
	s_mov_b32 s80, s54
	s_mov_b64 s[24:25], s[50:51]
	s_lshl_b32 s92, s17, 6
	v_readlane_b32 s55, v254, 44
	v_readlane_b32 s56, v254, 45
	v_readlane_b32 s57, v254, 46
	v_readlane_b32 s60, v254, 49
	v_readlane_b32 s61, v254, 50
.LBB0_1096:
	s_waitcnt lgkmcnt(0)
	s_barrier
	v_pk_mul_f32 v[212:213], v[80:81], v[82:83]
	ds_read_b128 v[80:83], v163
	v_pk_mul_f32 v[84:85], v[84:85], v[86:87]
	v_pk_mul_f32 v[180:181], v[88:89], v[90:91]
	v_bfe_u32 v86, v85, 16, 1
	v_bfe_u32 v87, v84, 16, 1
	v_add3_u32 v218, v84, v87, s3
	v_add3_u32 v219, v85, v86, s3
	ds_read_b128 v[84:87], v104 offset:55296
	ds_read_b128 v[88:91], v163 offset:64
	v_pk_mul_f32 v[92:93], v[92:93], v[94:95]
	s_waitcnt lgkmcnt(1)
	v_mfma_f32_16x16x32_bf16 v[80:83], v[80:83], v[84:87], 0
	v_bfe_u32 v68, v93, 16, 1
	s_mov_b64 exec, s[70:71]
	v_lshl_add_u64 v[248:249], v[248:249], 0, v[250:251]
	global_load_dwordx4 v[6:9], v[248:249], off
	s_mov_b64 exec, -1
	v_bfe_u32 v94, v92, 16, 1
	v_add3_u32 v220, v92, v94, s3
	v_add3_u32 v68, v93, v68, s3
	ds_read_b128 v[92:95], v104 offset:55360
	ds_read_b128 v[112:115], v163 offset:2304
	ds_read_b128 v[176:179], v163 offset:2368
	s_waitcnt lgkmcnt(2)
	v_mfma_f32_16x16x32_bf16 v[80:83], v[88:91], v[92:95], v[80:83]
	ds_read_b128 v[88:91], v163 offset:4608
	v_bfe_u32 v182, v180, 16, 1
	v_bfe_u32 v183, v181, 16, 1
	s_waitcnt lgkmcnt(2)
	v_mfma_f32_16x16x32_bf16 v[112:115], v[112:115], v[84:87], 0
	v_add3_u32 v223, v181, v183, s3
	v_add3_u32 v224, v180, v182, s3
	ds_read_b128 v[180:183], v163 offset:4672
	s_waitcnt lgkmcnt(2)
	v_mfma_f32_16x16x32_bf16 v[112:115], v[176:179], v[92:95], v[112:115]
	ds_read_b128 v[176:179], v148
	ds_read_b128 v[184:187], v149
	ds_read_b128 v[188:191], v163 offset:6912
	ds_read_b128 v[192:195], v163 offset:6976
	ds_read2_b64 v[196:199], v105 offset1:4
	ds_read_b128 v[200:203], v164
	s_mov_b64 exec, s[70:71]
	v_lshl_add_u64 v[248:249], v[248:249], 0, v[250:251]
	global_load_dwordx4 v[10:13], v[248:249], off
	s_mov_b64 exec, -1
	ds_read_b128 v[204:207], v164 offset:64
	v_bfe_u32 v221, v212, 16, 1
	s_waitcnt lgkmcnt(8)
; #define LAS __attribute__((address_space(3)))
; __device__ __forceinline__ unsigned f2bf(float f) { unsigned u = __builtin_bit_cast(unsigned, f); return (u + 0x7fffu + ((u >> 16) & 1u)) >> 16; }
; #define CBAR() do { asm volatile("s_waitcnt lgkmcnt(0)" ::: "memory"); __builtin_amdgcn_s_barrier(); asm volatile("" ::: "memory"); } while (0)
; __device__ __forceinline__ v2u pack4(const f32x4& v) { return (v2u){pg8::cvt_pk_bf16(v[0], v[1]), pg8::cvt_pk_bf16(v[2], v[3])}; }
; __device__ __forceinline__ void p4a_chunk(Frame& F0, const In& I) {
;     ...
;         for (int lvl = 0; lvl < 6; ++lvl) {
;             const int Wsrc = (lvl & 1) ? C_WB : C_WA, Wdst = (lvl & 1) ? C_WA : C_WB, Ms = (lvl & 1) ? C_MB : C_MA, Mts = (lvl & 1) ? C_MTB : C_MTA, Md = (lvl & 1) ? C_MA : C_MB, Mtd = (lvl & 1) ? C_MTA : C_MTB;
;             const Fr yW = LD(Wsrc, w); Fr yMt; if (lvl < 5) yMt = LD(Mts, nt);
;             Fr xM[4], xS[2];
; #pragma unroll
;             for (int i = 0; i < 4; ++i) xM[i] = LD(Ms, i);
;             if (lvl < 5) { xS[0] = LD(Ms, mt0); xS[1] = LD(Ms, mt0 + 1); }
;             const int nj = w * 16 + lr;
;             f32x4 old[4], aw[4], as[2];
; #pragma unroll
;             for (int i = 0; i < 4; ++i) old[i] = unpack4(*(const LAS v2u*)(L + Wsrc + nj * CP + (i * 16 + 4 * kq) * 2));
; #pragma unroll
;             for (int i = 0; i < 4; ++i) aw[i] = MM(xM[i], yW);
;             if (lvl < 5) {
; #pragma unroll
;                 for (int i = 0; i < 2; ++i) as[i] = MM(xS[i], yMt); }
; #pragma unroll
;             for (int i = 0; i < 4; ++i) *(LAS v2u*)(L + Wdst + nj * CP + (i * 16 + 4 * kq) * 2) = pack4(old[i] + aw[i]);
;             if (lvl < 5) {
; #pragma unroll
;                 for (int i = 0; i < 2; ++i) { const int m0 = (mt0 + i) * 16 + 4 * kq;
; #pragma unroll
;                     for (int e = 0; e < 4; ++e) *(LAS unsigned short*)(L + Md + (m0 + e) * CP + n * 2) = (unsigned short)f2bf(as[i][e]);
;                     if (lvl < 4) *(LAS v2u*)(L + Mtd + n * CP + m0 * 2) = pack4(as[i]); } }
;             if (lvl == 4) *(LAS v4u*)(L + C_KHT + lane * CP + 16 * w) = (v4u){kht[0], kht[1], kht[2], kht[3]};
;             if (lvl == 2) { if (hx) tr8_finish(tX, mX, tscr, lane);
;                             if (hy) { mX = moe_item(cit + 8, I.w_gu, I.w_down, F.ws); tr8_load(mX, tX, lane); } }
;             CBAR();
	v_mfma_f32_16x16x32_bf16 v[88:91], v[88:91], v[84:87], 0
	s_waitcnt lgkmcnt(2)
	v_lshlrev_b32_e32 v214, 16, v196
	v_and_b32_e32 v215, 0xffff0000, v196
	v_lshlrev_b32_e32 v196, 16, v197
	v_mfma_f32_16x16x32_bf16 v[84:87], v[188:191], v[84:87], 0
	v_and_b32_e32 v197, 0xffff0000, v197
	v_lshlrev_b32_e32 v216, 16, v198
	v_and_b32_e32 v217, 0xffff0000, v198
	v_mfma_f32_16x16x32_bf16 v[88:91], v[180:183], v[92:95], v[88:91]
	ds_read_b128 v[180:183], v165
	ds_read_b128 v[208:211], v165 offset:64
	v_pk_add_f32 v[82:83], v[82:83], v[196:197]
	v_pk_add_f32 v[80:81], v[80:81], v[214:215]
	v_mfma_f32_16x16x32_bf16 v[84:87], v[192:195], v[92:95], v[84:87]
	ds_read2_b64 v[92:95], v105 offset0:8 offset1:12
	v_lshlrev_b32_e32 v192, 16, v199
	v_and_b32_e32 v193, 0xffff0000, v199
	s_waitcnt lgkmcnt(4)
	v_mfma_f32_16x16x32_bf16 v[188:191], v[200:203], v[176:179], 0
	v_cvt_pk_bf16_f32 v80, v80, v81
	v_cvt_pk_bf16_f32 v81, v82, v83
	v_pk_add_f32 v[82:83], v[114:115], v[192:193]
	s_mov_b64 exec, s[70:71]
	v_lshl_add_u64 v[248:249], v[248:249], 0, v[250:251]
	global_load_dwordx4 v[14:17], v[248:249], off
	s_mov_b64 exec, -1
	s_waitcnt lgkmcnt(3)
	v_mfma_f32_16x16x32_bf16 v[188:191], v[204:207], v[184:187], v[188:191]
	v_add_f32_e64 v112, v112, v216
	v_add_f32_e64 v113, v113, v217
	s_waitcnt lgkmcnt(0)
	v_lshlrev_b32_e32 v194, 16, v92
	v_and_b32_e32 v195, 0xffff0000, v92
	v_lshlrev_b32_e32 v198, 16, v93
	v_and_b32_e32 v199, 0xffff0000, v93
	v_cvt_pk_bf16_f32 v112, v112, v113
	v_cvt_pk_bf16_f32 v113, v82, v83
	v_lshlrev_b32_e32 v200, 16, v94
	v_mfma_f32_16x16x32_bf16 v[176:179], v[180:183], v[176:179], 0
	v_and_b32_e32 v201, 0xffff0000, v94
	v_lshlrev_b32_e32 v180, 16, v95
	v_and_b32_e32 v181, 0xffff0000, v95
	ds_write2_b64 v103, v[80:81], v[112:113] offset1:4
	v_pk_add_f32 v[80:81], v[90:91], v[198:199]
	v_pk_add_f32 v[82:83], v[88:89], v[194:195]
	v_pk_add_f32 v[84:85], v[84:85], v[200:201]
	v_cvt_pk_bf16_f32 v82, v82, v83
	v_cvt_pk_bf16_f32 v83, v80, v81
	v_pk_add_f32 v[80:81], v[86:87], v[180:181]
	v_cvt_pk_bf16_f32 v84, v84, v85
	v_cvt_pk_bf16_f32 v85, v80, v81
	v_bfe_u32 v80, v188, 16, 1
	s_mov_b64 exec, s[70:71]
	v_lshl_add_u64 v[248:249], v[248:249], 0, v[250:251]
	global_load_dwordx4 v[18:21], v[248:249], off
	s_mov_b64 exec, -1
	v_add3_u32 v80, v188, v80, s3
	ds_write2_b64 v103, v[82:83], v[84:85] offset0:8 offset1:12
	ds_write_b16_d16_hi v108, v80
	v_bfe_u32 v80, v189, 16, 1
	v_add3_u32 v80, v189, v80, s3
	ds_write_b16_d16_hi v108, v80 offset:144
	v_bfe_u32 v80, v190, 16, 1
	v_mfma_f32_16x16x32_bf16 v[92:95], v[208:211], v[184:187], v[176:179]
	v_add3_u32 v80, v190, v80, s3
	ds_write_b16_d16_hi v108, v80 offset:288
	v_bfe_u32 v80, v191, 16, 1
	v_add3_u32 v80, v191, v80, s3
	ds_write_b16_d16_hi v108, v80 offset:432
	v_cvt_pk_bf16_f32 v80, v188, v189
	v_cvt_pk_bf16_f32 v81, v190, v191
	ds_write_b64 v110, v[80:81]
	v_bfe_u32 v80, v92, 16, 1
	v_add3_u32 v80, v92, v80, s3
	ds_write_b16_d16_hi v109, v80
	v_bfe_u32 v80, v93, 16, 1
	v_add3_u32 v80, v93, v80, s3
	ds_write_b16_d16_hi v109, v80 offset:144
	v_bfe_u32 v80, v94, 16, 1
	v_add3_u32 v80, v94, v80, s3
	ds_write_b16_d16_hi v109, v80 offset:288
	v_bfe_u32 v80, v95, 16, 1
	s_mov_b64 exec, s[70:71]
	v_lshl_add_u64 v[248:249], v[248:249], 0, v[250:251]
	global_load_dwordx4 v[22:25], v[248:249], off
	s_mov_b64 exec, -1
	v_add3_u32 v80, v95, v80, s3
	ds_write_b16_d16_hi v109, v80 offset:432
	v_cvt_pk_bf16_f32 v80, v92, v93
	v_cvt_pk_bf16_f32 v81, v94, v95
	ds_write_b64 v111, v[80:81]
	s_waitcnt lgkmcnt(0)
	s_barrier
	ds_read_b128 v[80:83], v160
	ds_read_b128 v[84:87], v104 offset:36864
	ds_read_b128 v[88:91], v160 offset:64
	v_bfe_u32 v222, v213, 16, 1
	v_add3_u32 v92, v213, v222, s3
	v_add3_u32 v93, v212, v221, s3
	v_lshrrev_b32_e32 v180, 16, v93
	v_lshrrev_b32_e32 v181, 16, v92
	ds_read_b128 v[92:95], v104 offset:36928
	ds_read_b128 v[108:111], v160 offset:2304
	s_waitcnt lgkmcnt(3)
	v_mfma_f32_16x16x32_bf16 v[80:83], v[80:83], v[84:87], 0
	ds_read_b128 v[112:115], v160 offset:2368
	v_lshrrev_b32_e32 v176, 16, v224
	v_lshrrev_b32_e32 v177, 16, v223
	s_waitcnt lgkmcnt(2)
	v_mfma_f32_16x16x32_bf16 v[80:83], v[88:91], v[92:95], v[80:83]
	v_and_or_b32 v91, v68, s4, v177
	v_and_or_b32 v90, v220, s4, v176
	s_mov_b64 exec, s[70:71]
	v_lshl_add_u64 v[248:249], v[248:249], 0, v[250:251]
	global_load_dwordx4 v[26:29], v[248:249], off
	s_mov_b64 exec, -1
	ds_read_b128 v[176:179], v160 offset:4608
	s_waitcnt lgkmcnt(2)
	v_mfma_f32_16x16x32_bf16 v[108:111], v[108:111], v[84:87], 0
	v_and_or_b32 v89, v219, s4, v181
	v_and_or_b32 v88, v218, s4, v180
	ds_read_b128 v[180:183], v160 offset:4672
	s_waitcnt lgkmcnt(2)
	v_mfma_f32_16x16x32_bf16 v[108:111], v[112:115], v[92:95], v[108:111]
	ds_read_b128 v[112:115], v144
	ds_read_b128 v[184:187], v145
	ds_read_b128 v[188:191], v160 offset:6912
	ds_read_b128 v[192:195], v160 offset:6976
	ds_read2_b64 v[196:199], v103 offset1:4
	ds_read_b128 v[200:203], v161
	ds_read_b128 v[204:207], v161 offset:64
	v_readlane_b32 s14, v255, 42
	s_waitcnt lgkmcnt(8)
	v_mfma_f32_16x16x32_bf16 v[176:179], v[176:179], v[84:87], 0
	s_waitcnt lgkmcnt(2)
	v_lshlrev_b32_e32 v212, 16, v196
	v_and_b32_e32 v213, 0xffff0000, v196
	v_lshlrev_b32_e32 v196, 16, v197
	v_mfma_f32_16x16x32_bf16 v[84:87], v[188:191], v[84:87], 0
	v_and_b32_e32 v197, 0xffff0000, v197
	v_lshlrev_b32_e32 v214, 16, v198
	v_and_b32_e32 v215, 0xffff0000, v198
	s_mov_b64 exec, s[70:71]
	v_lshl_add_u64 v[248:249], v[248:249], 0, v[250:251]
	global_load_dwordx4 v[30:33], v[248:249], off
	s_mov_b64 exec, -1
	s_waitcnt lgkmcnt(1)
; #define LAS __attribute__((address_space(3)))
; __device__ __forceinline__ unsigned f2bf(float f) { unsigned u = __builtin_bit_cast(unsigned, f); return (u + 0x7fffu + ((u >> 16) & 1u)) >> 16; }
; #define CBAR() do { asm volatile("s_waitcnt lgkmcnt(0)" ::: "memory"); __builtin_amdgcn_s_barrier(); asm volatile("" ::: "memory"); } while (0)
; __device__ __forceinline__ v2u pack4(const f32x4& v) { return (v2u){pg8::cvt_pk_bf16(v[0], v[1]), pg8::cvt_pk_bf16(v[2], v[3])}; }
; __device__ __forceinline__ void p4a_chunk(Frame& F0, const In& I) {
;     ...
;         for (int lvl = 0; lvl < 6; ++lvl) {
;             const int Wsrc = (lvl & 1) ? C_WB : C_WA, Wdst = (lvl & 1) ? C_WA : C_WB, Ms = (lvl & 1) ? C_MB : C_MA, Mts = (lvl & 1) ? C_MTB : C_MTA, Md = (lvl & 1) ? C_MA : C_MB, Mtd = (lvl & 1) ? C_MTA : C_MTB;
;             const Fr yW = LD(Wsrc, w); Fr yMt; if (lvl < 5) yMt = LD(Mts, nt);
;             Fr xM[4], xS[2];
; #pragma unroll
;             for (int i = 0; i < 4; ++i) xM[i] = LD(Ms, i);
;             if (lvl < 5) { xS[0] = LD(Ms, mt0); xS[1] = LD(Ms, mt0 + 1); }
;             const int nj = w * 16 + lr;
;             f32x4 old[4], aw[4], as[2];
; #pragma unroll
;             for (int i = 0; i < 4; ++i) old[i] = unpack4(*(const LAS v2u*)(L + Wsrc + nj * CP + (i * 16 + 4 * kq) * 2));
; #pragma unroll
;             for (int i = 0; i < 4; ++i) aw[i] = MM(xM[i], yW);
;             if (lvl < 5) {
; #pragma unroll
;                 for (int i = 0; i < 2; ++i) as[i] = MM(xS[i], yMt); }
; #pragma unroll
;             for (int i = 0; i < 4; ++i) *(LAS v2u*)(L + Wdst + nj * CP + (i * 16 + 4 * kq) * 2) = pack4(old[i] + aw[i]);
;             if (lvl < 5) {
; #pragma unroll
;                 for (int i = 0; i < 2; ++i) { const int m0 = (mt0 + i) * 16 + 4 * kq;
; #pragma unroll
;                     for (int e = 0; e < 4; ++e) *(LAS unsigned short*)(L + Md + (m0 + e) * CP + n * 2) = (unsigned short)f2bf(as[i][e]);
;                     if (lvl < 4) *(LAS v2u*)(L + Mtd + n * CP + m0 * 2) = pack4(as[i]); } }
;             if (lvl == 4) *(LAS v4u*)(L + C_KHT + lane * CP + 16 * w) = (v4u){kht[0], kht[1], kht[2], kht[3]};
;             if (lvl == 2) { if (hx) tr8_finish(tX, mX, tscr, lane);
;                             if (hy) { mX = moe_item(cit + 8, I.w_gu, I.w_down, F.ws); tr8_load(mX, tX, lane); } }
;             CBAR();
	v_mfma_f32_16x16x32_bf16 v[188:191], v[200:203], v[112:115], 0
	v_add_f32_e64 v82, v82, v196
	v_add_f32_e64 v83, v83, v197
	v_pk_add_f32 v[80:81], v[80:81], v[212:213]
	v_pk_add_f32 v[108:109], v[108:109], v[214:215]
	v_mfma_f32_16x16x32_bf16 v[176:179], v[180:183], v[92:95], v[176:179]
	ds_read_b128 v[180:183], v162
	ds_read_b128 v[208:211], v162 offset:64
	v_cvt_pk_bf16_f32 v80, v80, v81
	v_cvt_pk_bf16_f32 v81, v82, v83
	v_mfma_f32_16x16x32_bf16 v[84:87], v[192:195], v[92:95], v[84:87]
	ds_read2_b64 v[92:95], v103 offset0:8 offset1:12
	v_lshlrev_b32_e32 v192, 16, v199
	v_and_b32_e32 v193, 0xffff0000, v199
	s_waitcnt lgkmcnt(3)
	v_mfma_f32_16x16x32_bf16 v[188:191], v[204:207], v[184:187], v[188:191]
	v_add_f32_e64 v82, v110, v192
	v_add_f32_e64 v83, v111, v193
	s_waitcnt lgkmcnt(0)
	v_lshlrev_b32_e32 v194, 16, v92
	v_and_b32_e32 v195, 0xffff0000, v92
	v_lshlrev_b32_e32 v198, 16, v93
	v_and_b32_e32 v199, 0xffff0000, v93
	v_cvt_pk_bf16_f32 v108, v108, v109
	v_cvt_pk_bf16_f32 v109, v82, v83
	s_mov_b64 exec, s[70:71]
	v_lshl_add_u64 v[248:249], v[248:249], 0, v[250:251]
	global_load_dwordx4 v[34:37], v[248:249], off
	s_mov_b64 exec, -1
	v_lshlrev_b32_e32 v200, 16, v94
	v_mfma_f32_16x16x32_bf16 v[112:115], v[180:183], v[112:115], 0
	v_and_b32_e32 v201, 0xffff0000, v94
	v_lshlrev_b32_e32 v180, 16, v95
	v_and_b32_e32 v181, 0xffff0000, v95
	ds_write2_b64 v105, v[80:81], v[108:109] offset1:4
	v_pk_add_f32 v[80:81], v[178:179], v[198:199]
	v_pk_add_f32 v[82:83], v[176:177], v[194:195]
	v_pk_add_f32 v[84:85], v[84:85], v[200:201]
	v_cvt_pk_bf16_f32 v82, v82, v83
	v_cvt_pk_bf16_f32 v83, v80, v81
	v_pk_add_f32 v[80:81], v[86:87], v[180:181]
	v_bfe_u32 v68, v188, 16, 1
	v_cvt_pk_bf16_f32 v84, v84, v85
	v_cvt_pk_bf16_f32 v85, v80, v81
	v_add3_u32 v68, v188, v68, s3
	ds_write2_b64 v105, v[82:83], v[84:85] offset0:8 offset1:12
	ds_write_b16_d16_hi v106, v68
	v_bfe_u32 v68, v189, 16, 1
	v_add3_u32 v68, v189, v68, s3
	v_mfma_f32_16x16x32_bf16 v[92:95], v[208:211], v[184:187], v[112:115]
	ds_write_b16_d16_hi v106, v68 offset:144
	v_bfe_u32 v68, v190, 16, 1
	v_add3_u32 v68, v190, v68, s3
	ds_write_b16_d16_hi v106, v68 offset:288
	v_bfe_u32 v68, v191, 16, 1
	s_mov_b64 exec, s[70:71]
	v_lshl_add_u64 v[248:249], v[248:249], 0, v[250:251]
	global_load_dwordx4 v[38:41], v[248:249], off
	s_mov_b64 exec, -1
	v_add3_u32 v68, v191, v68, s3
	ds_write_b16_d16_hi v106, v68 offset:432
	s_nop 0
	v_bfe_u32 v68, v92, 16, 1
	v_add3_u32 v68, v92, v68, s3
	ds_write_b16_d16_hi v107, v68
	v_bfe_u32 v68, v93, 16, 1
	v_add3_u32 v68, v93, v68, s3
	ds_write_b16_d16_hi v107, v68 offset:144
	v_bfe_u32 v68, v94, 16, 1
	v_add3_u32 v68, v94, v68, s3
	ds_write_b16_d16_hi v107, v68 offset:288
	v_bfe_u32 v68, v95, 16, 1
	v_add3_u32 v68, v95, v68, s3
	ds_write_b16_d16_hi v107, v68 offset:432
	ds_write_b128 v157, v[88:91]
	s_waitcnt lgkmcnt(0)
	s_barrier
	ds_read_b128 v[80:83], v163
	ds_read_b128 v[84:87], v163 offset:64
	ds_read_b128 v[88:91], v104 offset:55296
	ds_read_b128 v[92:95], v104 offset:55360
	s_waitcnt lgkmcnt(1)
	v_mfma_f32_16x16x32_bf16 v[80:83], v[80:83], v[88:91], 0
	ds_read_b128 v[106:109], v163 offset:2304
	ds_read_b128 v[110:113], v163 offset:4608
	v_lshlrev_b32_e32 v104, 16, v171
	s_waitcnt lgkmcnt(2)
	v_mfma_f32_16x16x32_bf16 v[80:83], v[84:87], v[92:95], v[80:83]
	ds_read_b128 v[84:87], v163 offset:2368
	v_lshlrev_b32_e32 v68, 16, v169
	v_readlane_b32 s15, v255, 43
	s_mov_b64 exec, s[70:71]
	v_lshl_add_u64 v[248:249], v[248:249], 0, v[250:251]
	global_load_dwordx4 v[42:45], v[248:249], off
	s_mov_b64 exec, -1
	s_waitcnt lgkmcnt(2)
	v_mfma_f32_16x16x32_bf16 v[106:109], v[106:109], v[88:91], 0
	s_waitcnt lgkmcnt(0)
	v_mfma_f32_16x16x32_bf16 v[84:87], v[84:87], v[92:95], v[106:109]
	s_nop 5
	ds_read_b128 v[106:109], v163 offset:4672
	ds_read_b128 v[176:179], v163 offset:6912
	ds_read_b128 v[180:183], v163 offset:6976
	v_mfma_f32_16x16x32_bf16 v[110:113], v[110:113], v[88:91], 0
	s_waitcnt lgkmcnt(1)
	v_mfma_f32_16x16x32_bf16 v[88:91], v[176:179], v[88:91], 0
	ds_read2_b64 v[176:179], v105 offset0:8 offset1:12
	s_waitcnt lgkmcnt(0)
	v_and_b32_e32 v171, 0xffff0000, v177
	v_mfma_f32_16x16x32_bf16 v[106:109], v[106:109], v[92:95], v[110:113]
	v_lshlrev_b32_e32 v114, 16, v178
	v_and_b32_e32 v115, 0xffff0000, v178
	v_and_b32_e32 v169, 0xffff0000, v179
	v_mfma_f32_16x16x32_bf16 v[88:91], v[180:183], v[92:95], v[88:91]
	ds_read2_b64 v[92:95], v105 offset1:4
	s_mov_b64 exec, s[70:71]
	v_lshl_add_u64 v[248:249], v[248:249], 0, v[250:251]
	global_load_dwordx4 v[46:49], v[248:249], off
	s_mov_b64 exec, -1
	v_lshlrev_b32_e32 v113, 16, v175
	v_lshlrev_b32_e32 v112, 16, v173
	v_or_b32_sdwa v113, v113, v174 dst_sel:DWORD dst_unused:UNUSED_PAD src0_sel:DWORD src1_sel:WORD_0
	v_or_b32_sdwa v112, v112, v172 dst_sel:DWORD dst_unused:UNUSED_PAD src0_sel:DWORD src1_sel:WORD_0
	s_waitcnt lgkmcnt(0)
	v_lshlrev_b32_e32 v174, 16, v92
	v_and_b32_e32 v175, 0xffff0000, v92
	v_lshlrev_b32_e32 v92, 16, v93
	v_and_b32_e32 v93, 0xffff0000, v93
	v_lshlrev_b32_e32 v172, 16, v94
	v_and_b32_e32 v173, 0xffff0000, v94
	v_lshlrev_b32_e32 v94, 16, v95
	v_and_b32_e32 v95, 0xffff0000, v95
	v_pk_add_f32 v[82:83], v[82:83], v[92:93]
	v_pk_add_f32 v[80:81], v[80:81], v[174:175]
	v_pk_add_f32 v[84:85], v[84:85], v[172:173]
	v_cvt_pk_bf16_f32 v80, v80, v81
	v_cvt_pk_bf16_f32 v81, v82, v83
	v_pk_add_f32 v[82:83], v[86:87], v[94:95]
	v_or_b32_sdwa v111, v104, v170 dst_sel:DWORD dst_unused:UNUSED_PAD src0_sel:DWORD src1_sel:WORD_0
	v_lshlrev_b32_e32 v104, 16, v176
	v_and_b32_e32 v105, 0xffff0000, v176
	v_lshlrev_b32_e32 v170, 16, v177
	v_cvt_pk_bf16_f32 v84, v84, v85
	v_cvt_pk_bf16_f32 v85, v82, v83
	v_or_b32_sdwa v110, v68, v168 dst_sel:DWORD dst_unused:UNUSED_PAD src0_sel:DWORD src1_sel:WORD_0
	s_mov_b64 exec, s[70:71]
	v_lshl_add_u64 v[248:249], v[248:249], 0, v[250:251]
	global_load_dwordx4 v[50:53], v[248:249], off
	s_mov_b64 exec, -1
	v_lshlrev_b32_e32 v168, 16, v179
	ds_write2_b64 v103, v[80:81], v[84:85] offset1:4
	v_pk_add_f32 v[80:81], v[108:109], v[170:171]
	v_pk_add_f32 v[82:83], v[106:107], v[104:105]
	v_pk_add_f32 v[84:85], v[88:89], v[114:115]
	v_cvt_pk_bf16_f32 v82, v82, v83
	v_cvt_pk_bf16_f32 v83, v80, v81
	v_pk_add_f32 v[80:81], v[90:91], v[168:169]
	v_cvt_pk_bf16_f32 v84, v84, v85
	v_cvt_pk_bf16_f32 v85, v80, v81
	ds_write2_b64 v103, v[82:83], v[84:85] offset0:8 offset1:12
	s_waitcnt lgkmcnt(0)
	s_barrier
; #define GAS __attribute__((address_space(1)))
; #define LAS __attribute__((address_space(3)))
; __device__ __forceinline__ v2u pack4(const f32x4& v) { return (v2u){pg8::cvt_pk_bf16(v[0], v[1]), pg8::cvt_pk_bf16(v[2], v[3])}; }
; __device__ __forceinline__ f32x4 unpack4(const v2u w) { return (f32x4){bflo(w.x), bfhi(w.x), bflo(w.y), bfhi(w.y)}; }
; __device__ __forceinline__ void p4a_chunk(Frame& F0, const In& I) {
;     ...
;         *(LAS v4u*)(L + C_VT + lane * CP + 16 * w) = (v4u){vtt[0], vtt[1], vtt[2], vtt[3]};
;         unsigned char* og = CHK + (size_t)unit * CHK_UNIT_BYTES;
;         { const Fr yW1 = LD(C_WA, nt), yW2 = LD(C_WA + 64 * CP, nt);
;           Fr xA[2], xK[2];
; #pragma unroll
;           for (int i = 0; i < 2; ++i) { xA[i] = LD(C_ATT, mt0 + i); xK[i] = LD(C_AAK, mt0 + i); }
;           f32x4 rv[2], av[2], kv[2];
;           const float gm = ((const LAS float*)(L + C_GAM))[n];
; #pragma unroll
;           for (int i = 0; i < 2; ++i) { const int m0 = (mt0 + i) * 16 + 4 * kq;
;               rv[i] = unpack4(*(const LAS v2u*)(L + C_RT + n * CP + m0 * 2)); av[i] = unpack4(*(const LAS v2u*)(L + C_ARKT + n * CP + m0 * 2)); kv[i] = unpack4(*(const LAS v2u*)(L + C_KHT + n * CP + m0 * 2)); }
;           f32x4 p7[2], p8[2], p9[2], p10[2];
; #pragma unroll
;           for (int i = 0; i < 2; ++i) { p7[i] = MM(xA[i], yW1); p8[i] = MM(xK[i], yW1); p9[i] = MM(xA[i], yW2); p10[i] = MM(xK[i], yW2); }
; #pragma unroll
;           for (int i = 0; i < 2; ++i) { const int m0 = (mt0 + i) * 16 + 4 * kq;
;               *(GAS v2u*)(og + 0 * 8192 + n * 128 + m0 * 2) = pack4(p7[i] + rv[i]);
;               *(LAS v2u*)(L + C_QYT + n * CP + m0 * 2) = pack4(p8[i] + av[i]);
;               f32x4 v = p9[i];
; #pragma unroll
;               for (int e = 0; e < 4; ++e) v[e] += (m0 + e == n) ? gm : 0.f;
;               *(GAS v2u*)(og + 1 * 8192 + n * 128 + m0 * 2) = pack4(v);
;               *(LAS v2u*)(L + C_QST + n * CP + m0 * 2) = pack4(p10[i] + kv[i]); } }
	ds_write_b128 v158, v[110:113] offset:55296
	ds_read_b128 v[80:83], v96 offset:9216
	ds_read_b128 v[84:87], v123 offset:36864
	ds_read_b128 v[88:91], v96 offset:9280
	ds_read_b128 v[92:95], v96 offset:18432
	ds_read_b32 v68, v136
	ds_read_b128 v[104:107], v123 offset:46144
	ds_read_b128 v[112:115], v123 offset:36928
	ds_read_b128 v[168:171], v123 offset:46080
	s_waitcnt lgkmcnt(6)
	v_mfma_f32_16x16x32_bf16 v[108:111], v[80:83], v[84:87], 0
	v_add_u32_e32 v103, v121, v70
	ds_read_b128 v[176:179], v96 offset:18496
	s_mov_b64 exec, s[70:71]
	v_lshl_add_u64 v[248:249], v[248:249], 0, v[250:251]
	global_load_dwordx4 v[54:57], v[248:249], off
	s_mov_b64 exec, -1
	ds_read_b128 v[180:183], v97 offset:9216
	ds_read2st64_b64 v[184:187], v103 offset1:54
	ds_read_b128 v[188:191], v97 offset:9280
	ds_read_b128 v[192:195], v97 offset:18432
	s_waitcnt lgkmcnt(5)
	v_mfma_f32_16x16x32_bf16 v[80:83], v[80:83], v[168:171], 0
	v_add_u32_e32 v103, v137, v70
	s_waitcnt lgkmcnt(2)
	v_lshlrev_b32_e32 v196, 16, v184
	v_and_b32_e32 v197, 0xffff0000, v184
	v_mfma_f32_16x16x32_bf16 v[108:111], v[88:91], v[112:115], v[108:111]
	v_lshlrev_b32_e32 v198, 16, v185
	v_and_b32_e32 v199, 0xffff0000, v185
	v_lshlrev_b32_e32 v200, 16, v186
	v_mfma_f32_16x16x32_bf16 v[172:175], v[92:95], v[84:87], 0
	v_and_b32_e32 v201, 0xffff0000, v186
	v_lshlrev_b32_e32 v204, 16, v187
	v_and_b32_e32 v205, 0xffff0000, v187
	v_mfma_f32_16x16x32_bf16 v[80:83], v[88:91], v[104:107], v[80:83]
	v_mfma_f32_16x16x32_bf16 v[88:91], v[92:95], v[168:171], 0
	ds_read_b128 v[92:95], v97 offset:18496
	ds_read_b64 v[202:203], v103
	v_add_u32_e32 v103, v121, v72
	ds_read2st64_b64 v[184:187], v103 offset1:54
	v_mfma_f32_16x16x32_bf16 v[172:175], v[176:179], v[112:115], v[172:175]
	v_add_u32_e32 v103, v137, v72
	s_mov_b64 exec, s[70:71]
	v_lshl_add_u64 v[248:249], v[248:249], 0, v[250:251]
	global_load_dwordx4 v[58:61], v[248:249], off
	s_mov_b64 exec, -1
	s_waitcnt lgkmcnt(1)
	v_lshlrev_b32_e32 v206, 16, v202
	v_and_b32_e32 v207, 0xffff0000, v202
	v_mfma_f32_16x16x32_bf16 v[88:91], v[176:179], v[104:107], v[88:91]
	v_lshlrev_b32_e32 v202, 16, v203
	v_and_b32_e32 v203, 0xffff0000, v203
	s_waitcnt lgkmcnt(0)
	v_lshlrev_b32_e32 v208, 16, v184
	v_mfma_f32_16x16x32_bf16 v[176:179], v[180:183], v[84:87], 0
	v_and_b32_e32 v209, 0xffff0000, v184
	v_lshlrev_b32_e32 v184, 16, v185
	v_and_b32_e32 v185, 0xffff0000, v185
	v_mfma_f32_16x16x32_bf16 v[84:87], v[192:195], v[84:87], 0
	v_lshlrev_b32_e32 v210, 16, v186
	v_and_b32_e32 v211, 0xffff0000, v186
	v_mfma_f32_16x16x32_bf16 v[176:179], v[188:191], v[112:115], v[176:179]
	v_mfma_f32_16x16x32_bf16 v[84:87], v[92:95], v[112:115], v[84:87]
	v_mfma_f32_16x16x32_bf16 v[112:115], v[180:183], v[168:171], 0
	ds_read_b64 v[180:181], v103
	v_lshlrev_b32_e32 v182, 16, v187
	v_and_b32_e32 v183, 0xffff0000, v187
	v_mfma_f32_16x16x32_bf16 v[168:171], v[192:195], v[168:171], 0
	v_add_u32_e32 v103, v138, v141
	s_waitcnt lgkmcnt(0)
	v_lshlrev_b32_e32 v186, 16, v180
	v_and_b32_e32 v187, 0xffff0000, v180
	v_mfma_f32_16x16x32_bf16 v[112:115], v[188:191], v[104:107], v[112:115]
	v_lshl_add_u64 v[188:189], v[76:77], 0, v[74:75]
	s_mov_b64 exec, s[70:71]
	v_lshl_add_u64 v[248:249], v[248:249], 0, v[250:251]
	global_load_dwordx4 v[62:65], v[248:249], off
	s_mov_b64 exec, -1
	v_lshlrev_b32_e32 v180, 16, v181
	v_and_b32_e32 v181, 0xffff0000, v181
	v_mfma_f32_16x16x32_bf16 v[92:95], v[92:95], v[104:107], v[168:171]
	v_add_f32_e64 v104, v110, v198
	v_add_f32_e64 v105, v111, v199
	v_pk_add_f32 v[106:107], v[108:109], v[196:197]
	s_nop 0
	v_cvt_pk_bf16_f32 v106, v106, v107
	v_cvt_pk_bf16_f32 v107, v104, v105
	v_add_co_u32_e32 v104, vcc, s10, v188
	s_nop 1
	v_addc_co_u32_e32 v105, vcc, 0, v189, vcc
	global_store_dwordx2 v[104:105], v[106:107], off
	v_pk_add_f32 v[104:105], v[174:175], v[204:205]
	v_pk_add_f32 v[106:107], v[172:173], v[200:201]
	v_lshl_add_u64 v[172:173], v[78:79], 0, v[74:75]
	v_cvt_pk_bf16_f32 v106, v106, v107
	v_cvt_pk_bf16_f32 v107, v104, v105
	v_cndmask_b32_e64 v105, 0, v68, s[38:39]
	v_cndmask_b32_e64 v104, 0, v68, s[36:37]
	v_pk_add_f32 v[80:81], v[104:105], v[80:81]
	v_cndmask_b32_e64 v105, 0, v68, s[40:41]
	v_cndmask_b32_e64 v104, 0, v68, s[14:15]
	v_pk_add_f32 v[82:83], v[104:105], v[82:83]
	v_cvt_pk_bf16_f32 v80, v80, v81
	v_cvt_pk_bf16_f32 v81, v82, v83
	v_add_co_u32_e32 v82, vcc, s11, v188
	v_readlane_b32 s14, v255, 46
	s_nop 0
	v_addc_co_u32_e32 v83, vcc, 0, v189, vcc
	global_store_dwordx2 v[82:83], v[80:81], off
	v_pk_add_f32 v[80:81], v[90:91], v[202:203]
	v_pk_add_f32 v[82:83], v[88:89], v[206:207]
	v_readlane_b32 s15, v255, 47
	v_cvt_pk_bf16_f32 v82, v82, v83
	v_cvt_pk_bf16_f32 v83, v80, v81
	ds_write_b64 v99, v[82:83]
	v_pk_add_f32 v[80:81], v[178:179], v[184:185]
	v_pk_add_f32 v[82:83], v[176:177], v[208:209]
	ds_write_b64 v103, v[106:107]
	v_cvt_pk_bf16_f32 v82, v82, v83
	v_cvt_pk_bf16_f32 v83, v80, v81
	v_add_co_u32_e32 v80, vcc, s10, v172
	s_nop 1
	v_addc_co_u32_e32 v81, vcc, 0, v173, vcc
	global_store_dwordx2 v[80:81], v[82:83], off
	v_pk_add_f32 v[80:81], v[86:87], v[182:183]
	v_pk_add_f32 v[82:83], v[84:85], v[210:211]
	s_nop 0
	v_cvt_pk_bf16_f32 v82, v82, v83
	v_cvt_pk_bf16_f32 v83, v80, v81
	v_cndmask_b32_e64 v81, 0, v68, s[14:15]
	v_readlane_b32 s14, v255, 44
	v_add_u32_e32 v80, v138, v143
	v_readlane_b32 s15, v255, 45
	ds_write_b64 v80, v[82:83]
	s_nop 0
	v_cndmask_b32_e64 v80, 0, v68, s[14:15]
	v_readlane_b32 s14, v255, 48
	v_readlane_b32 s15, v255, 49
	v_pk_add_f32 v[80:81], v[80:81], v[112:113]
	s_nop 0
	v_cndmask_b32_e64 v83, 0, v68, s[14:15]
	v_readlane_b32 s14, v255, 50
	v_readlane_b32 s15, v255, 51
	v_cvt_pk_bf16_f32 v80, v80, v81
	s_nop 0
	v_cndmask_b32_e64 v82, 0, v68, s[14:15]
	v_pk_add_f32 v[82:83], v[82:83], v[114:115]
	v_add_u32_e32 v68, v138, v122
	v_cvt_pk_bf16_f32 v81, v82, v83
	v_add_co_u32_e32 v82, vcc, s11, v172
	s_mov_b32 s14, 0xd8006000
	s_nop 0
	v_addc_co_u32_e32 v83, vcc, 0, v173, vcc
	global_store_dwordx2 v[82:83], v[80:81], off
	v_pk_add_f32 v[80:81], v[94:95], v[180:181]
	v_pk_add_f32 v[82:83], v[92:93], v[186:187]
	s_nop 0
	v_cvt_pk_bf16_f32 v82, v82, v83
	v_cvt_pk_bf16_f32 v83, v80, v81
	ds_write_b64 v98, v[82:83]
	s_waitcnt lgkmcnt(0)
	s_barrier
; __device__ __forceinline__ void tr8_finish(const f32x4 (&v)[16], const MoeItem& m, LAS float* scr_, int lane) {
;     LAS unsigned char* scr = (LAS unsigned char*)scr_;
;     const int kr = lane >> 4, cq = lane & 15;
; #pragma unroll
;     for (int j = 0; j < 4; ++j) { unsigned w[4];
; #pragma unroll
;         for (int q = 0; q < 4; ++q) { s16x2 t = {0, 0};
;             t = __builtin_amdgcn_cvt_scalef32_pk_fp8_f32(t, v[4 * q][j], v[4 * q + 1][j], F8_CVT_SCALE, false);
;             t = __builtin_amdgcn_cvt_scalef32_pk_fp8_f32(t, v[4 * q + 2][j], v[4 * q + 3][j], F8_CVT_SCALE, true);
;             w[q] = __builtin_bit_cast(unsigned, t); }
;         *(LAS v4u*)(scr + (4 * cq + j) * 80 + kr * 16) = (v4u){w[0], w[1], w[2], w[3]}; }
;     LDS_WAIT(); asm volatile("" ::: "memory");
;     const int qd = lane & 3;
; #pragma unroll
;     for (int ps = 0; ps < 4; ++ps) { const int n = (lane >> 2) + 16 * ps; const LAS unsigned char* s = scr + n * 80 + qd * 4;
;         const unsigned d0 = *(const LAS unsigned*)(s), d1 = *(const LAS unsigned*)(s + 16), d2 = *(const LAS unsigned*)(s + 32), d3 = *(const LAS unsigned*)(s + 48);
;         const unsigned t0 = __builtin_amdgcn_perm(d1, d0, 0x05010400u), t1 = __builtin_amdgcn_perm(d1, d0, 0x07030602u), t2 = __builtin_amdgcn_perm(d3, d2, 0x05010400u), t3 = __builtin_amdgcn_perm(d3, d2, 0x07030602u);
;         const v4u o = (v4u){__builtin_amdgcn_perm(t2, t0, 0x05040100u), __builtin_amdgcn_perm(t2, t0, 0x07060302u), __builtin_amdgcn_perm(t3, t1, 0x05040100u), __builtin_amdgcn_perm(t3, t1, 0x07060302u)};
;         *(GAS v4u*)(m.WT + (size_t)(m.drow + n) * m.ldt + m.k0 + 16 * qd) = o; }
;     LDS_WAIT(); asm volatile("" ::: "memory");
; }
; __device__ __forceinline__ void p4a_chunk(Frame& F0, const In& I) {
;     ...
;         { const Fr yQy = LD(C_QYT, nt), yQs = LD(C_QST, nt);
;           Fr xV[2];
; #pragma unroll
;           for (int i = 0; i < 2; ++i) xV[i] = LD(C_VT, mt0 + i);
;           f32x4 p11[2], p12[2];
; #pragma unroll
;           for (int i = 0; i < 2; ++i) { p11[i] = MM(xV[i], yQy); p12[i] = MM(xV[i], yQs); }
; #pragma unroll
;           for (int i = 0; i < 2; ++i) { const int m0 = (mt0 + i) * 16 + 4 * kq;
;               *(GAS v2u*)(og + 2 * 8192 + n * 128 + m0 * 2) = pack4(p11[i]);
;               *(GAS v2u*)(og + 3 * 8192 + n * 128 + m0 * 2) = pack4(p12[i]); } }
;         if (hy) tr8_finish(tX, mX, tscr, lane);
	ds_read_b128 v[80:83], v96 offset:55296
	ds_read_b128 v[84:87], v96 offset:55360
	ds_read_b128 v[88:91], v68
	ds_read_b128 v[92:95], v68 offset:64
	v_add_u32_e32 v68, v127, v122
	ds_read_b128 v[108:111], v68
	ds_read_b128 v[112:115], v68 offset:64
	s_waitcnt lgkmcnt(3)
	v_mfma_f32_16x16x32_bf16 v[104:107], v[80:83], v[88:91], 0
	ds_read_b128 v[168:171], v97 offset:55296
	s_waitcnt lgkmcnt(2)
	v_mfma_f32_16x16x32_bf16 v[80:83], v[80:83], v[108:111], 0
	v_mfma_f32_16x16x32_bf16 v[104:107], v[84:87], v[92:95], v[104:107]
	s_waitcnt lgkmcnt(1)
	v_mfma_f32_16x16x32_bf16 v[80:83], v[84:87], v[112:115], v[80:83]
	ds_read_b128 v[84:87], v97 offset:55360
	s_waitcnt lgkmcnt(1)
	v_mfma_f32_16x16x32_bf16 v[88:91], v[168:171], v[88:91], 0
	s_waitcnt lgkmcnt(0)
	v_mfma_f32_16x16x32_bf16 v[88:91], v[84:87], v[92:95], v[88:91]
	s_nop 2
	v_cvt_pk_bf16_f32 v80, v80, v81
	v_cvt_pk_bf16_f32 v81, v82, v83
	v_mfma_f32_16x16x32_bf16 v[92:95], v[168:171], v[108:111], 0
	v_mfma_f32_16x16x32_bf16 v[84:87], v[84:87], v[112:115], v[92:95]
	s_nop 6
	v_add_co_u32_e32 v94, vcc, s12, v188
	v_cvt_pk_bf16_f32 v92, v104, v105
	s_nop 0
	v_addc_co_u32_e32 v95, vcc, 0, v189, vcc
	v_add_co_u32_e32 v82, vcc, s14, v188
	v_cvt_pk_bf16_f32 v93, v106, v107
	s_nop 0
	v_addc_co_u32_e32 v83, vcc, 0, v189, vcc
	global_store_dwordx2 v[82:83], v[80:81], off
	v_add_co_u32_e32 v82, vcc, s12, v172
	v_cvt_pk_bf16_f32 v80, v88, v89
	v_cvt_pk_bf16_f32 v81, v90, v91
	v_addc_co_u32_e32 v83, vcc, 0, v173, vcc
	global_store_dwordx2 v[94:95], v[92:93], off
	global_store_dwordx2 v[82:83], v[80:81], off
	v_add_co_u32_e32 v82, vcc, 0xd8006000, v172
	v_cvt_pk_bf16_f32 v80, v84, v85
	s_nop 0
	v_addc_co_u32_e32 v83, vcc, 0, v173, vcc
	v_cvt_pk_bf16_f32 v81, v86, v87
	s_and_b64 vcc, exec, s[64:65]
	global_store_dwordx2 v[82:83], v[80:81], off
	s_cbranch_vccnz .LBB0_1082
	v_mov_b32_e32 v80, v69
	v_mov_b32_e32 v81, v69
	v_mov_b32_e32 v82, v69
	v_mov_b32_e32 v83, v69
	s_waitcnt vmcnt(18)
	v_cvt_scalef32_pk_fp8_f32 v80, v2, v6, s5
	v_cvt_scalef32_pk_fp8_f32 v81, v18, v22, s5
	s_waitcnt vmcnt(14)
	v_cvt_scalef32_pk_fp8_f32 v82, v34, v38, s5
	s_waitcnt vmcnt(10)
	v_cvt_scalef32_pk_fp8_f32 v83, v50, v54, s5
	v_cvt_scalef32_pk_fp8_f32 v80, v10, v14, s5 op_sel:[0,0,0,1]
	v_cvt_scalef32_pk_fp8_f32 v81, v26, v30, s5 op_sel:[0,0,0,1]
	v_cvt_scalef32_pk_fp8_f32 v82, v42, v46, s5 op_sel:[0,0,0,1]
	s_waitcnt vmcnt(8)
	v_cvt_scalef32_pk_fp8_f32 v83, v58, v62, s5 op_sel:[0,0,0,1]
	ds_write_b128 v166, v[80:83]
	v_mov_b32_e32 v80, v69
	v_mov_b32_e32 v81, v69
	v_mov_b32_e32 v82, v69
	v_mov_b32_e32 v83, v69
	v_cvt_scalef32_pk_fp8_f32 v80, v3, v7, s5
	v_cvt_scalef32_pk_fp8_f32 v81, v19, v23, s5
	v_cvt_scalef32_pk_fp8_f32 v82, v35, v39, s5
	v_cvt_scalef32_pk_fp8_f32 v83, v51, v55, s5
	v_cvt_scalef32_pk_fp8_f32 v80, v11, v15, s5 op_sel:[0,0,0,1]
	v_cvt_scalef32_pk_fp8_f32 v81, v27, v31, s5 op_sel:[0,0,0,1]
	v_cvt_scalef32_pk_fp8_f32 v82, v43, v47, s5 op_sel:[0,0,0,1]
	v_cvt_scalef32_pk_fp8_f32 v83, v59, v63, s5 op_sel:[0,0,0,1]
	ds_write_b128 v166, v[80:83] offset:80
	v_mov_b32_e32 v80, v69
	v_mov_b32_e32 v81, v69
	v_mov_b32_e32 v82, v69
	v_mov_b32_e32 v83, v69
	v_cvt_scalef32_pk_fp8_f32 v80, v4, v8, s5
	v_cvt_scalef32_pk_fp8_f32 v81, v20, v24, s5
	v_cvt_scalef32_pk_fp8_f32 v82, v36, v40, s5
	v_cvt_scalef32_pk_fp8_f32 v83, v52, v56, s5
	v_cvt_scalef32_pk_fp8_f32 v80, v12, v16, s5 op_sel:[0,0,0,1]
	v_cvt_scalef32_pk_fp8_f32 v81, v28, v32, s5 op_sel:[0,0,0,1]
	v_cvt_scalef32_pk_fp8_f32 v82, v44, v48, s5 op_sel:[0,0,0,1]
	v_cvt_scalef32_pk_fp8_f32 v83, v60, v64, s5 op_sel:[0,0,0,1]
	ds_write_b128 v166, v[80:83] offset:160
	v_mov_b32_e32 v80, v69
	v_mov_b32_e32 v81, v69
	v_mov_b32_e32 v82, v69
	v_mov_b32_e32 v83, v69
	v_cvt_scalef32_pk_fp8_f32 v80, v5, v9, s5
	v_cvt_scalef32_pk_fp8_f32 v81, v21, v25, s5
	v_cvt_scalef32_pk_fp8_f32 v82, v37, v41, s5
	v_cvt_scalef32_pk_fp8_f32 v83, v53, v57, s5
	v_cvt_scalef32_pk_fp8_f32 v80, v13, v17, s5 op_sel:[0,0,0,1]
	v_cvt_scalef32_pk_fp8_f32 v81, v29, v33, s5 op_sel:[0,0,0,1]
	v_cvt_scalef32_pk_fp8_f32 v82, v45, v49, s5 op_sel:[0,0,0,1]
	v_cvt_scalef32_pk_fp8_f32 v83, v61, v65, s5 op_sel:[0,0,0,1]
	ds_write_b128 v166, v[80:83] offset:240
	s_waitcnt lgkmcnt(0)
	ds_read2_b32 v[80:81], v167 offset1:4
	ds_read2_b32 v[82:83], v167 offset0:8 offset1:12
	s_ashr_i32 s93, s92, 31
	s_waitcnt lgkmcnt(1)
	v_perm_b32 v68, v81, v80, s6
	v_perm_b32 v84, v81, v80, s7
	s_waitcnt lgkmcnt(0)
	v_perm_b32 v81, v83, v82, s6
	v_perm_b32 v83, v83, v82, s7
	v_perm_b32 v80, v81, v68, s8
	v_perm_b32 v81, v81, v68, s9
	v_add_u32_e32 v68, s86, v132
	v_perm_b32 v82, v83, v84, s8
	v_perm_b32 v83, v83, v84, s9
	v_lshlrev_b64 v[84:85], 11, v[68:69]
	v_lshl_add_u64 v[84:85], s[72:73], 0, v[84:85]
	v_lshl_add_u64 v[84:85], v[84:85], 0, s[92:93]
	v_lshl_add_u64 v[84:85], v[84:85], 0, v[66:67]
	global_store_dwordx4 v[84:85], v[80:83], off
	ds_read2_b32 v[80:81], v102 offset0:64 offset1:68
	ds_read2_b32 v[82:83], v102 offset0:72 offset1:76
	s_waitcnt lgkmcnt(1)
	v_perm_b32 v68, v81, v80, s6
	v_perm_b32 v84, v81, v80, s7
	s_waitcnt lgkmcnt(0)
	v_perm_b32 v81, v83, v82, s6
	v_perm_b32 v83, v83, v82, s7
	v_perm_b32 v80, v81, v68, s8
	v_perm_b32 v81, v81, v68, s9
	v_add_u32_e32 v68, s86, v133
	v_perm_b32 v82, v83, v84, s8
	v_perm_b32 v83, v83, v84, s9
	v_lshlrev_b64 v[84:85], 11, v[68:69]
	v_lshl_add_u64 v[84:85], s[72:73], 0, v[84:85]
	v_lshl_add_u64 v[84:85], v[84:85], 0, s[92:93]
	v_lshl_add_u64 v[84:85], v[84:85], 0, v[66:67]
	global_store_dwordx4 v[84:85], v[80:83], off
	ds_read2_b32 v[80:81], v101 offset0:128 offset1:132
	ds_read2_b32 v[82:83], v101 offset0:136 offset1:140
	s_waitcnt lgkmcnt(1)
	v_perm_b32 v68, v81, v80, s6
	v_perm_b32 v84, v81, v80, s7
	s_waitcnt lgkmcnt(0)
	v_perm_b32 v81, v83, v82, s6
	v_perm_b32 v83, v83, v82, s7
	v_perm_b32 v80, v81, v68, s8
	v_perm_b32 v81, v81, v68, s9
	v_add_u32_e32 v68, s86, v134
	v_perm_b32 v82, v83, v84, s8
	v_perm_b32 v83, v83, v84, s9
	v_lshlrev_b64 v[84:85], 11, v[68:69]
	v_lshl_add_u64 v[84:85], s[72:73], 0, v[84:85]
	v_lshl_add_u64 v[84:85], v[84:85], 0, s[92:93]
	v_lshl_add_u64 v[84:85], v[84:85], 0, v[66:67]
	global_store_dwordx4 v[84:85], v[80:83], off
	ds_read2_b32 v[80:81], v100 offset0:192 offset1:196
	ds_read2_b32 v[82:83], v100 offset0:200 offset1:204
	s_waitcnt lgkmcnt(1)
	v_perm_b32 v68, v81, v80, s6
	v_perm_b32 v84, v81, v80, s7
	s_waitcnt lgkmcnt(0)
	v_perm_b32 v81, v83, v82, s6
	v_perm_b32 v83, v83, v82, s7
	v_perm_b32 v80, v81, v68, s8
	v_perm_b32 v81, v81, v68, s9
	v_add_u32_e32 v68, s86, v135
	v_perm_b32 v82, v83, v84, s8
	v_perm_b32 v83, v83, v84, s9
	v_lshlrev_b64 v[84:85], 11, v[68:69]
	v_lshl_add_u64 v[84:85], s[72:73], 0, v[84:85]
	v_lshl_add_u64 v[84:85], v[84:85], 0, s[92:93]
	v_lshl_add_u64 v[84:85], v[84:85], 0, v[66:67]
	global_store_dwordx4 v[84:85], v[80:83], off
	s_waitcnt lgkmcnt(0)
	s_branch .LBB0_1082
